# attention: drop redundant negm copies and canonicalising maxes
# speedup vs baseline: 1.0058x; 1.0058x over previous
; __device__ __forceinline__ void qkt64c(f32x16& p0, f32x16& p1, const char* Ks, const bf16x8* qr, const f32x16& cinit, int r32, int hi) {
; #pragma unroll
;     for (int d0 = 0; d0 < 4; ++d0) { const int cb = (d0 * 16 + hi * 8) * 2;
;         const bf16x8 b0 = *reinterpret_cast<const bf16x8*>(Ks + kswz<64>(r32, cb));
;         const bf16x8 b1 = *reinterpret_cast<const bf16x8*>(Ks + kswz<64>(32 + r32, cb));
;         if (d0 == 0) { p0 = __builtin_amdgcn_mfma_f32_32x32x16_bf16(b0, qr[0], cinit, 0, 0, 0); p1 = __builtin_amdgcn_mfma_f32_32x32x16_bf16(b1, qr[0], cinit, 0, 0, 0); }
;         else { p0 = __builtin_amdgcn_mfma_f32_32x32x16_bf16(b0, qr[d0], p0, 0, 0, 0); p1 = __builtin_amdgcn_mfma_f32_32x32x16_bf16(b1, qr[d0], p1, 0, 0, 0); } }
; }
.LBB0_823:
	v_lshl_add_u64 v[202:203], v[200:201], 0, s[64:65]
	s_mov_b32 s2, 0x8a40000
	v_add_co_u32_e32 v64, vcc, s2, v202
	s_mov_b32 s2, 0x8a50000
	s_nop 0
	v_addc_co_u32_e32 v65, vcc, 0, v203, vcc
	v_add_co_u32_e32 v66, vcc, s2, v202
	v_lshl_add_u64 v[204:205], v[198:199], 0, s[64:65]
	s_nop 0
	v_addc_co_u32_e32 v67, vcc, 0, v203, vcc
	s_mov_b32 s2, 0x6a40000
	global_load_dwordx4 v[178:181], v[64:65], off
	global_load_dwordx4 v[182:185], v[66:67], off
	v_add_co_u32_e32 v64, vcc, s2, v204
	s_nop 1
	v_addc_co_u32_e32 v65, vcc, 0, v205, vcc
	global_load_dwordx4 v[186:189], v[64:65], off
	s_lshl_b32 s2, s42, 13
	s_add_i32 s2, s2, 0
	v_add_u32_e32 v128, s2, v223
	ds_read_b128 v[232:235], v128 offset:53248
	ds_read_b128 v[144:147], v128 offset:49152
	v_exp_f32_e32 v190, v120
	v_exp_f32_e32 v191, v121
	v_add_f32_e32 v120, v96, v97
	v_add_f32_e32 v121, v98, v99
	s_waitcnt lgkmcnt(0)
	v_mfma_f32_32x32x16_bf16 v[128:143], v[144:147], v[162:165], v[80:95]
	v_add_u32_e32 v144, s2, v226
	ds_read_b128 v[236:239], v144 offset:53248
	ds_read_b128 v[144:147], v144 offset:49152
	v_exp_f32_e32 v192, v122
	v_add_f32_e32 v120, v120, v121
	v_add_f32_e32 v121, v100, v101
	v_add_f32_e32 v122, v102, v103
	v_exp_f32_e32 v193, v123
	s_waitcnt lgkmcnt(0)
	v_mfma_f32_32x32x16_bf16 v[128:143], v[144:147], v[166:169], v[128:143]
	v_add_u32_e32 v144, s2, v228
	ds_read_b128 v[240:243], v144 offset:53248
	ds_read_b128 v[144:147], v144 offset:49152
	v_add_f32_e32 v121, v121, v122
	v_add_f32_e32 v122, v104, v105
	v_add_f32_e32 v123, v106, v107
	v_add_f32_e32 v122, v122, v123
	v_add_f32_e32 v123, v108, v109
	s_waitcnt lgkmcnt(0)
	v_mfma_f32_32x32x16_bf16 v[128:143], v[144:147], v[170:173], v[128:143]
	v_add_u32_e32 v144, s2, v229
	ds_read_b128 v[244:247], v144 offset:53248
	ds_read_b128 v[144:147], v144 offset:49152
	v_add_f32_e32 v208, v110, v111
	v_add_f32_e32 v123, v123, v208
	v_add_f32_e32 v208, v112, v113
	v_add_f32_e32 v209, v114, v115
	v_add_f32_e32 v208, v208, v209
	s_waitcnt lgkmcnt(0)
	v_mfma_f32_32x32x16_bf16 v[128:143], v[144:147], v[174:177], v[128:143]
	v_exp_f32_e32 v124, v124
	v_exp_f32_e32 v125, v125
	v_mfma_f32_32x32x16_bf16 v[144:159], v[232:235], v[162:165], v[80:95]
	v_exp_f32_e32 v126, v126
	v_exp_f32_e32 v127, v127
	v_add_f32_e32 v120, v208, v120
	v_add_f32_e32 v208, v116, v117
	v_add_f32_e32 v209, v118, v119
	v_add_f32_e32 v208, v208, v209
	v_add_f32_e32 v121, v208, v121
	v_mfma_f32_32x32x16_bf16 v[144:159], v[236:239], v[166:169], v[144:159]
	v_add_f32_e32 v208, v190, v191
	v_add_f32_e32 v209, v192, v193
	v_add_f32_e32 v208, v208, v209
	v_add_f32_e32 v122, v122, v208
	v_add_f32_e32 v208, v124, v125
	v_add_f32_e32 v209, v126, v127
	v_add_f32_e32 v208, v208, v209
	v_mfma_f32_32x32x16_bf16 v[144:159], v[240:243], v[170:173], v[144:159]
	v_add_f32_e32 v123, v123, v208
	v_add_f32_e32 v120, v120, v121
	v_add_f32_e32 v121, v122, v123
	v_add_f32_e32 v231, v120, v121
	v_mov_b32_e32 v232, v231
	v_cvt_pk_bf16_f32 v96, v96, v97
	v_cvt_pk_bf16_f32 v97, v98, v99
	v_mfma_f32_32x32x16_bf16 v[144:159], v[244:247], v[174:177], v[144:159]
	v_cvt_pk_bf16_f32 v98, v100, v101
	v_cvt_pk_bf16_f32 v99, v102, v103
	v_cvt_pk_bf16_f32 v120, v104, v105
	v_cvt_pk_bf16_f32 v121, v106, v107
	v_cvt_pk_bf16_f32 v122, v108, v109
	v_cvt_pk_bf16_f32 v123, v110, v111
	v_cvt_pk_bf16_f32 v104, v112, v113
	v_cvt_pk_bf16_f32 v105, v114, v115
	v_cvt_pk_bf16_f32 v106, v116, v117
	v_cvt_pk_bf16_f32 v107, v118, v119
	v_cvt_pk_bf16_f32 v100, v190, v191
	v_cvt_pk_bf16_f32 v101, v192, v193
	v_cvt_pk_bf16_f32 v102, v124, v125
	v_cvt_pk_bf16_f32 v103, v126, v127
	s_nop 0
	v_permlane32_swap_b32_e32 v231, v232
	v_permlane32_swap_b32_e32 v96, v98
	v_permlane32_swap_b32_e32 v97, v99
	v_permlane32_swap_b32_e32 v120, v122
	v_permlane32_swap_b32_e32 v121, v123
	v_permlane32_swap_b32_e32 v104, v106
	v_permlane32_swap_b32_e32 v105, v107
	v_permlane32_swap_b32_e32 v100, v102
	v_permlane32_swap_b32_e32 v101, v103
	v_lshl_add_u32 v234, s12, 14, v217
	ds_read_b64_tr_b16 v[108:109], v234 offset:0
	ds_read_b64_tr_b16 v[110:111], v234 offset:0x800
	ds_read_b64_tr_b16 v[112:113], v234 offset:0x1000
	ds_read_b64_tr_b16 v[114:115], v234 offset:0x1800
	ds_read_b64_tr_b16 v[116:117], v234 offset:0x2000
	ds_read_b64_tr_b16 v[118:119], v234 offset:0x2800
	ds_read_b64_tr_b16 v[124:125], v234 offset:0x3000
	ds_read_b64_tr_b16 v[126:127], v234 offset:0x3800
	ds_read_b64_tr_b16 v[236:237], v234 offset:0x200
	ds_read_b64_tr_b16 v[238:239], v234 offset:0xa00
	ds_read_b64_tr_b16 v[240:241], v234 offset:0x1200
	ds_read_b64_tr_b16 v[242:243], v234 offset:0x1a00
	ds_read_b64_tr_b16 v[244:245], v234 offset:0x2200
	ds_read_b64_tr_b16 v[246:247], v234 offset:0x2a00
	ds_read_b64_tr_b16 v[190:191], v234 offset:0x3200
	ds_read_b64_tr_b16 v[192:193], v234 offset:0x3a00
	s_waitcnt lgkmcnt(8)
	s_nop 0
	v_mfma_f32_32x32x16_bf16 v[0:15], v[96:99], v[108:111], v[0:15]
	v_max_f32_e32 v108, v128, v129
	v_max3_f32 v109, v130, v131, v145
	v_max3_f32 v108, v108, v144, v146
	v_max3_f32 v108, v108, v147, v132
	v_max3_f32 v109, v109, v134, v135
	v_mfma_f32_32x32x16_bf16 v[0:15], v[120:123], v[112:115], v[0:15]
	v_max3_f32 v208, v108, v133, v148
	v_max3_f32 v209, v109, v150, v151
	v_mfma_f32_32x32x16_bf16 v[0:15], v[104:107], v[116:119], v[0:15]
	v_mfma_f32_32x32x16_bf16 v[0:15], v[100:103], v[124:127], v[0:15]
	ds_read_b64_tr_b16 v[124:125], v234 offset:0x400
	ds_read_b64_tr_b16 v[126:127], v234 offset:0xc00
	ds_read_b64_tr_b16 v[116:117], v234 offset:0x1400
	ds_read_b64_tr_b16 v[118:119], v234 offset:0x1c00
	ds_read_b64_tr_b16 v[112:113], v234 offset:0x2400
	ds_read_b64_tr_b16 v[114:115], v234 offset:0x2c00
	ds_read_b64_tr_b16 v[108:109], v234 offset:0x3400
	ds_read_b64_tr_b16 v[110:111], v234 offset:0x3c00
	s_waitcnt lgkmcnt(8)
	v_mfma_f32_32x32x16_bf16 v[48:63], v[96:99], v[236:239], v[48:63]
	v_max3_f32 v208, v208, v149, v136
	v_max3_f32 v209, v209, v138, v139
	v_max3_f32 v208, v208, v137, v152
	v_max3_f32 v209, v209, v154, v155
	v_max3_f32 v208, v208, v153, v140
	v_max3_f32 v209, v209, v142, v143
	v_max3_f32 v208, v208, v141, v156
	v_mfma_f32_32x32x16_bf16 v[48:63], v[120:123], v[240:243], v[48:63]
	v_max3_f32 v209, v209, v158, v159
	v_max3_f32 v208, v208, v157, v209
	v_mov_b32_e32 v209, v208
	s_nop 1
	v_permlane32_swap_b32_e32 v208, v209
	v_mfma_f32_32x32x16_bf16 v[48:63], v[104:107], v[244:247], v[48:63]
	v_max_f32_e32 v233, v208, v209
	v_mfma_f32_32x32x16_bf16 v[48:63], v[100:103], v[190:193], v[48:63]
	s_mov_b32 s2, 0x4138aa3b
	v_cmp_ge_f32_e32 vcc, s2, v233
	s_cmp_eq_u64 vcc, exec
	s_cbranch_scc0 .LBB0_836
	v_mov_b32_e32 v233, 1.0

; __device__ __forceinline__ void qkt64c(f32x16& p0, f32x16& p1, const char* Ks, const bf16x8* qr, const f32x16& cinit, int r32, int hi) {
; #pragma unroll
;     for (int d0 = 0; d0 < 4; ++d0) { const int cb = (d0 * 16 + hi * 8) * 2;
;         const bf16x8 b0 = *reinterpret_cast<const bf16x8*>(Ks + kswz<64>(r32, cb));
;         const bf16x8 b1 = *reinterpret_cast<const bf16x8*>(Ks + kswz<64>(32 + r32, cb));
;         if (d0 == 0) { p0 = __builtin_amdgcn_mfma_f32_32x32x16_bf16(b0, qr[0], cinit, 0, 0, 0); p1 = __builtin_amdgcn_mfma_f32_32x32x16_bf16(b1, qr[0], cinit, 0, 0, 0); }
;         else { p0 = __builtin_amdgcn_mfma_f32_32x32x16_bf16(b0, qr[d0], p0, 0, 0, 0); p1 = __builtin_amdgcn_mfma_f32_32x32x16_bf16(b1, qr[d0], p1, 0, 0, 0); } }
; }
.LBB0_829:
	v_add_co_u32_e32 v96, vcc, 0x8a60000, v202
	s_waitcnt lgkmcnt(0)
	s_nop 0
	v_addc_co_u32_e32 v97, vcc, 0, v203, vcc
	v_add_co_u32_e32 v98, vcc, 0x8a70000, v202
	s_barrier
	s_nop 0
	v_addc_co_u32_e32 v99, vcc, 0, v203, vcc
	global_load_dwordx4 v[178:181], v[96:97], off
	global_load_dwordx4 v[182:185], v[98:99], off
	v_add_co_u32_e32 v96, vcc, 0x6a60000, v204
	s_nop 1
	v_addc_co_u32_e32 v97, vcc, 0, v205, vcc
	global_load_dwordx4 v[186:189], v[96:97], off
	v_add_u32_e32 v96, s2, v223
	ds_read_b128 v[190:193], v96 offset:53248
	ds_read_b128 v[112:115], v96 offset:49152
	v_exp_f32_e32 v208, v152
	v_exp_f32_e32 v209, v153
	v_add_f32_e32 v152, v128, v129
	v_add_f32_e32 v153, v130, v131
	s_waitcnt lgkmcnt(0)
	v_mfma_f32_32x32x16_bf16 v[96:111], v[112:115], v[162:165], v[80:95]
	v_add_u32_e32 v112, s2, v226
	ds_read_b128 v[202:205], v112 offset:53248
	ds_read_b128 v[112:115], v112 offset:49152
	v_exp_f32_e32 v210, v154
	v_add_f32_e32 v152, v152, v153
	v_add_f32_e32 v153, v132, v133
	v_add_f32_e32 v154, v134, v135
	v_exp_f32_e32 v211, v155
	s_waitcnt lgkmcnt(0)
	v_mfma_f32_32x32x16_bf16 v[96:111], v[112:115], v[166:169], v[96:111]
	v_add_u32_e32 v112, s2, v228
	ds_read_b128 v[234:237], v112 offset:53248
	ds_read_b128 v[112:115], v112 offset:49152
	v_add_f32_e32 v153, v153, v154
	v_add_f32_e32 v154, v136, v137
	v_add_f32_e32 v155, v138, v139
	v_add_f32_e32 v154, v154, v155
	v_add_f32_e32 v155, v140, v141
	s_waitcnt lgkmcnt(0)
	v_mfma_f32_32x32x16_bf16 v[96:111], v[112:115], v[170:173], v[96:111]
	v_add_u32_e32 v112, s2, v229
	ds_read_b128 v[238:241], v112 offset:53248
	ds_read_b128 v[112:115], v112 offset:49152
	v_exp_f32_e32 v156, v156
	v_exp_f32_e32 v157, v157
	v_exp_f32_e32 v158, v158
	v_exp_f32_e32 v159, v159
	s_waitcnt lgkmcnt(0)
	v_mfma_f32_32x32x16_bf16 v[96:111], v[112:115], v[174:177], v[96:111]
	v_mfma_f32_32x32x16_bf16 v[112:127], v[190:193], v[162:165], v[80:95]
	v_add_f32_e32 v190, v142, v143
	v_add_f32_e32 v155, v155, v190
	v_add_f32_e32 v190, v144, v145
	v_add_f32_e32 v191, v146, v147
	v_add_f32_e32 v190, v190, v191
	v_add_f32_e32 v152, v152, v190
	v_add_f32_e32 v190, v148, v149
	v_mfma_f32_32x32x16_bf16 v[112:127], v[202:205], v[166:169], v[112:127]
	v_add_f32_e32 v191, v150, v151
	v_add_f32_e32 v190, v190, v191
	v_add_f32_e32 v153, v153, v190
	v_add_f32_e32 v190, v208, v209
	v_add_f32_e32 v191, v210, v211
	v_add_f32_e32 v190, v190, v191
	v_add_f32_e32 v154, v154, v190
	v_mfma_f32_32x32x16_bf16 v[112:127], v[234:237], v[170:173], v[112:127]
	v_add_f32_e32 v190, v156, v157
	v_add_f32_e32 v191, v158, v159
	v_add_f32_e32 v190, v190, v191
	v_add_f32_e32 v155, v155, v190
	v_add_f32_e32 v152, v152, v153
	v_add_f32_e32 v153, v154, v155
	v_add_f32_e32 v203, v152, v153
	v_mfma_f32_32x32x16_bf16 v[112:127], v[238:241], v[174:177], v[112:127]
	v_mov_b32_e32 v204, v203
	v_cvt_pk_bf16_f32 v152, v128, v129
	v_cvt_pk_bf16_f32 v153, v130, v131
	v_cvt_pk_bf16_f32 v154, v132, v133
	v_cvt_pk_bf16_f32 v155, v134, v135
	v_cvt_pk_bf16_f32 v136, v136, v137
	v_cvt_pk_bf16_f32 v137, v138, v139
	v_cvt_pk_bf16_f32 v138, v140, v141
	v_cvt_pk_bf16_f32 v139, v142, v143
	v_cvt_pk_bf16_f32 v132, v144, v145
	v_cvt_pk_bf16_f32 v133, v146, v147
	v_cvt_pk_bf16_f32 v134, v148, v149
	v_cvt_pk_bf16_f32 v135, v150, v151
	v_cvt_pk_bf16_f32 v128, v208, v209
	v_cvt_pk_bf16_f32 v129, v210, v211
	v_cvt_pk_bf16_f32 v130, v156, v157
	v_cvt_pk_bf16_f32 v131, v158, v159
	s_nop 1
	v_permlane32_swap_b32_e32 v203, v204
	v_permlane32_swap_b32_e32 v152, v154
	v_permlane32_swap_b32_e32 v153, v155
	v_permlane32_swap_b32_e32 v136, v138
	v_permlane32_swap_b32_e32 v137, v139
	v_permlane32_swap_b32_e32 v132, v134
	v_permlane32_swap_b32_e32 v133, v135
	v_permlane32_swap_b32_e32 v128, v130
	v_permlane32_swap_b32_e32 v129, v131
	v_lshl_add_u32 v205, s42, 14, v217
	ds_read_b64_tr_b16 v[140:141], v205 offset:0
	ds_read_b64_tr_b16 v[142:143], v205 offset:0x800
	ds_read_b64_tr_b16 v[144:145], v205 offset:0x1000
	ds_read_b64_tr_b16 v[146:147], v205 offset:0x1800
	ds_read_b64_tr_b16 v[148:149], v205 offset:0x2000
	ds_read_b64_tr_b16 v[150:151], v205 offset:0x2800
	ds_read_b64_tr_b16 v[156:157], v205 offset:0x3000
	ds_read_b64_tr_b16 v[158:159], v205 offset:0x3800
	ds_read_b64_tr_b16 v[190:191], v205 offset:0x200
	ds_read_b64_tr_b16 v[192:193], v205 offset:0xa00
	ds_read_b64_tr_b16 v[234:235], v205 offset:0x1200
	ds_read_b64_tr_b16 v[236:237], v205 offset:0x1a00
	ds_read_b64_tr_b16 v[238:239], v205 offset:0x2200
	ds_read_b64_tr_b16 v[240:241], v205 offset:0x2a00
	ds_read_b64_tr_b16 v[242:243], v205 offset:0x3200
	ds_read_b64_tr_b16 v[244:245], v205 offset:0x3a00
	s_waitcnt lgkmcnt(8)
	s_nop 0
	v_mfma_f32_32x32x16_bf16 v[0:15], v[152:155], v[140:143], v[0:15]
	v_max_f32_e32 v140, v96, v97
	v_max3_f32 v140, v140, v112, v114
	v_max3_f32 v141, v98, v99, v113
	v_max3_f32 v140, v140, v115, v100
	v_max3_f32 v141, v141, v102, v103
	v_mfma_f32_32x32x16_bf16 v[0:15], v[136:139], v[144:147], v[0:15]
	v_max3_f32 v202, v140, v101, v116
	v_max3_f32 v208, v141, v118, v119
	v_mfma_f32_32x32x16_bf16 v[0:15], v[132:135], v[148:151], v[0:15]
	v_mfma_f32_32x32x16_bf16 v[0:15], v[128:131], v[156:159], v[0:15]
	ds_read_b64_tr_b16 v[156:157], v205 offset:0x400
	ds_read_b64_tr_b16 v[158:159], v205 offset:0xc00
	ds_read_b64_tr_b16 v[148:149], v205 offset:0x1400
	ds_read_b64_tr_b16 v[150:151], v205 offset:0x1c00
	ds_read_b64_tr_b16 v[144:145], v205 offset:0x2400
	ds_read_b64_tr_b16 v[146:147], v205 offset:0x2c00
	ds_read_b64_tr_b16 v[140:141], v205 offset:0x3400
	ds_read_b64_tr_b16 v[142:143], v205 offset:0x3c00
	s_waitcnt lgkmcnt(8)
	v_mfma_f32_32x32x16_bf16 v[48:63], v[152:155], v[190:193], v[48:63]
	v_max3_f32 v190, v202, v117, v104
	v_max3_f32 v191, v208, v106, v107
	v_max3_f32 v190, v190, v105, v120
	v_max3_f32 v191, v191, v122, v123
	v_max3_f32 v190, v190, v121, v108
	v_max3_f32 v191, v191, v110, v111
	v_max3_f32 v190, v190, v109, v124
	v_mfma_f32_32x32x16_bf16 v[48:63], v[136:139], v[234:237], v[48:63]
	v_max3_f32 v191, v191, v126, v127
	v_max3_f32 v190, v190, v125, v191
	v_mov_b32_e32 v191, v190
	s_nop 1
	v_permlane32_swap_b32_e32 v190, v191
	v_mfma_f32_32x32x16_bf16 v[48:63], v[132:135], v[238:241], v[48:63]
	v_max_f32_e32 v234, v190, v191
	v_mfma_f32_32x32x16_bf16 v[48:63], v[128:131], v[242:245], v[48:63]
	s_mov_b32 s2, 0x4138aa3b
	v_cmp_ge_f32_e32 vcc, s2, v234
	s_cmp_eq_u64 vcc, exec
	v_mov_b32_e32 v202, 1.0
	s_cbranch_scc0 .LBB0_837

; __device__ __forceinline__ void qkt64c(f32x16& p0, f32x16& p1, const char* Ks, const bf16x8* qr, const f32x16& cinit, int r32, int hi) {
; #pragma unroll
;     for (int d0 = 0; d0 < 4; ++d0) { const int cb = (d0 * 16 + hi * 8) * 2;
;         const bf16x8 b0 = *reinterpret_cast<const bf16x8*>(Ks + kswz<64>(r32, cb));
;         const bf16x8 b1 = *reinterpret_cast<const bf16x8*>(Ks + kswz<64>(32 + r32, cb));
;         if (d0 == 0) { p0 = __builtin_amdgcn_mfma_f32_32x32x16_bf16(b0, qr[0], cinit, 0, 0, 0); p1 = __builtin_amdgcn_mfma_f32_32x32x16_bf16(b1, qr[0], cinit, 0, 0, 0); }
;         else { p0 = __builtin_amdgcn_mfma_f32_32x32x16_bf16(b0, qr[d0], p0, 0, 0, 0); p1 = __builtin_amdgcn_mfma_f32_32x32x16_bf16(b1, qr[d0], p1, 0, 0, 0); } }
; }
.LBB0_838:
	v_mov_b64_e32 v[64:65], v[80:81]
	v_mov_b64_e32 v[66:67], v[82:83]
	v_mov_b64_e32 v[68:69], v[84:85]
	v_mov_b64_e32 v[70:71], v[86:87]
	v_mov_b64_e32 v[72:73], v[88:89]
	v_mov_b64_e32 v[74:75], v[90:91]
	v_mov_b64_e32 v[76:77], v[92:93]
	v_mov_b64_e32 v[78:79], v[94:95]
	ds_read_b128 v[128:131], v222 offset:61440
	ds_read_b128 v[132:135], v222 offset:57344
	v_exp_f32_e32 v124, v124
	v_exp_f32_e32 v125, v125
	v_exp_f32_e32 v126, v126
	v_exp_f32_e32 v127, v127
	s_waitcnt lgkmcnt(0)
	v_mfma_f32_32x32x16_bf16 v[80:95], v[132:135], v[162:165], v[64:79]
	ds_read_b128 v[132:135], v224 offset:61440
	ds_read_b128 v[136:139], v224 offset:57344
	s_waitcnt lgkmcnt(0)
	v_mfma_f32_32x32x16_bf16 v[80:95], v[136:139], v[166:169], v[80:95]
	ds_read_b128 v[136:139], v225 offset:61440
	ds_read_b128 v[140:143], v225 offset:57344
	v_mfma_f32_32x32x16_bf16 v[64:79], v[128:131], v[162:165], v[64:79]
	v_add_f32_e32 v128, v110, v111
	v_add_f32_e32 v129, v114, v115
	s_waitcnt lgkmcnt(0)
	v_mfma_f32_32x32x16_bf16 v[80:95], v[140:143], v[170:173], v[80:95]
	ds_read_b128 v[140:143], v227 offset:61440
	ds_read_b128 v[144:147], v227 offset:57344
	v_mfma_f32_32x32x16_bf16 v[64:79], v[132:135], v[166:169], v[64:79]
	s_waitcnt lgkmcnt(0)
	v_mfma_f32_32x32x16_bf16 v[80:95], v[144:147], v[174:177], v[80:95]
	v_exp_f32_e32 v144, v120
	v_exp_f32_e32 v145, v121
	v_add_f32_e32 v120, v96, v97
	v_add_f32_e32 v121, v98, v99
	v_exp_f32_e32 v146, v122
	v_add_f32_e32 v120, v120, v121
	v_add_f32_e32 v121, v100, v101
	v_mfma_f32_32x32x16_bf16 v[64:79], v[136:139], v[170:173], v[64:79]
	v_add_f32_e32 v122, v102, v103
	v_exp_f32_e32 v147, v123
	v_add_f32_e32 v121, v121, v122
	v_add_f32_e32 v122, v104, v105
	v_add_f32_e32 v123, v106, v107
	v_add_f32_e32 v122, v122, v123
	v_add_f32_e32 v123, v108, v109
	v_add_f32_e32 v123, v123, v128
	v_add_f32_e32 v128, v112, v113
	v_add_f32_e32 v128, v128, v129
	v_add_f32_e32 v120, v120, v128
	v_add_f32_e32 v128, v116, v117
	v_add_f32_e32 v129, v118, v119
	v_add_f32_e32 v128, v128, v129
	v_add_f32_e32 v121, v121, v128
	v_add_f32_e32 v128, v144, v145
	v_add_f32_e32 v129, v146, v147
	v_mfma_f32_32x32x16_bf16 v[64:79], v[140:143], v[174:177], v[64:79]
	v_add_f32_e32 v128, v128, v129
	v_add_f32_e32 v122, v122, v128
	v_add_f32_e32 v128, v124, v125
	v_add_f32_e32 v129, v126, v127
	v_add_f32_e32 v128, v128, v129
	v_add_f32_e32 v123, v123, v128
	v_add_f32_e32 v120, v120, v121
	v_add_f32_e32 v121, v122, v123
	v_add_f32_e32 v128, v120, v121
	v_mov_b32_e32 v129, v128
	v_cvt_pk_bf16_f32 v96, v96, v97
	v_cvt_pk_bf16_f32 v97, v98, v99
	v_cvt_pk_bf16_f32 v98, v100, v101
	v_cvt_pk_bf16_f32 v99, v102, v103
	v_cvt_pk_bf16_f32 v120, v104, v105
	v_cvt_pk_bf16_f32 v121, v106, v107
	v_cvt_pk_bf16_f32 v122, v108, v109
	v_cvt_pk_bf16_f32 v123, v110, v111
	v_cvt_pk_bf16_f32 v104, v112, v113
	v_cvt_pk_bf16_f32 v105, v114, v115
	v_cvt_pk_bf16_f32 v106, v116, v117
	v_cvt_pk_bf16_f32 v107, v118, v119
	v_cvt_pk_bf16_f32 v100, v144, v145
	v_cvt_pk_bf16_f32 v101, v146, v147
	v_cvt_pk_bf16_f32 v102, v124, v125
	v_cvt_pk_bf16_f32 v103, v126, v127
	s_nop 1
	v_permlane32_swap_b32_e32 v128, v129
	v_permlane32_swap_b32_e32 v96, v98
	v_permlane32_swap_b32_e32 v97, v99
	v_permlane32_swap_b32_e32 v120, v122
	v_permlane32_swap_b32_e32 v121, v123
	v_permlane32_swap_b32_e32 v104, v106
	v_permlane32_swap_b32_e32 v105, v107
	v_permlane32_swap_b32_e32 v100, v102
	v_permlane32_swap_b32_e32 v101, v103
	ds_read_b64_tr_b16 v[108:109], v217 offset:0
	ds_read_b64_tr_b16 v[110:111], v217 offset:0x800
	ds_read_b64_tr_b16 v[112:113], v217 offset:0x1000
	ds_read_b64_tr_b16 v[114:115], v217 offset:0x1800
	ds_read_b64_tr_b16 v[116:117], v217 offset:0x2000
	ds_read_b64_tr_b16 v[118:119], v217 offset:0x2800
	ds_read_b64_tr_b16 v[124:125], v217 offset:0x3000
	ds_read_b64_tr_b16 v[126:127], v217 offset:0x3800
	ds_read_b64_tr_b16 v[130:131], v217 offset:0x200
	ds_read_b64_tr_b16 v[132:133], v217 offset:0xa00
	ds_read_b64_tr_b16 v[134:135], v217 offset:0x1200
	ds_read_b64_tr_b16 v[136:137], v217 offset:0x1a00
	ds_read_b64_tr_b16 v[138:139], v217 offset:0x2200
	ds_read_b64_tr_b16 v[140:141], v217 offset:0x2a00
	ds_read_b64_tr_b16 v[142:143], v217 offset:0x3200
	ds_read_b64_tr_b16 v[144:145], v217 offset:0x3a00
	s_waitcnt lgkmcnt(8)
	s_nop 0
	v_mfma_f32_32x32x16_bf16 v[0:15], v[96:99], v[108:111], v[0:15]
	v_max_f32_e32 v108, v81, v81
	v_max_f32_e32 v109, v80, v80
	v_max_f32_e32 v108, v109, v108
	v_max3_f32 v109, v82, v83, v65
	v_max3_f32 v108, v108, v64, v66
	v_max3_f32 v108, v108, v67, v84
	v_max3_f32 v109, v109, v86, v87
	v_mfma_f32_32x32x16_bf16 v[0:15], v[120:123], v[112:115], v[0:15]
	v_max3_f32 v146, v108, v85, v68
	v_max3_f32 v147, v109, v70, v71
	v_mfma_f32_32x32x16_bf16 v[0:15], v[104:107], v[116:119], v[0:15]
	v_mfma_f32_32x32x16_bf16 v[0:15], v[100:103], v[124:127], v[0:15]
	ds_read_b64_tr_b16 v[124:125], v217 offset:0x400
	ds_read_b64_tr_b16 v[126:127], v217 offset:0xc00
	ds_read_b64_tr_b16 v[116:117], v217 offset:0x1400
	ds_read_b64_tr_b16 v[118:119], v217 offset:0x1c00
	ds_read_b64_tr_b16 v[112:113], v217 offset:0x2400
	ds_read_b64_tr_b16 v[114:115], v217 offset:0x2c00
	ds_read_b64_tr_b16 v[108:109], v217 offset:0x3400
	ds_read_b64_tr_b16 v[110:111], v217 offset:0x3c00
	s_waitcnt lgkmcnt(8)
	v_mfma_f32_32x32x16_bf16 v[48:63], v[96:99], v[130:133], v[48:63]
	v_max3_f32 v130, v146, v69, v88
	v_max3_f32 v131, v147, v90, v91
	v_max3_f32 v130, v130, v89, v72
	v_max3_f32 v131, v131, v74, v75
	v_max3_f32 v130, v130, v73, v92
	v_max3_f32 v131, v131, v94, v95
	v_max3_f32 v130, v130, v93, v76
	v_mfma_f32_32x32x16_bf16 v[48:63], v[120:123], v[134:137], v[48:63]
	v_max3_f32 v131, v131, v78, v79
	v_max3_f32 v130, v130, v77, v131
	v_mov_b32_e32 v131, v130
	s_nop 1
	v_permlane32_swap_b32_e32 v130, v131
	v_max_f32_e32 v131, v131, v131
	v_max_f32_e32 v130, v130, v130
	v_mfma_f32_32x32x16_bf16 v[48:63], v[104:107], v[138:141], v[48:63]
	v_max_f32_e32 v131, v130, v131
	v_mfma_f32_32x32x16_bf16 v[48:63], v[100:103], v[142:145], v[48:63]
	s_mov_b32 s2, 0x4138aa3b
	v_cmp_ge_f32_e32 vcc, s2, v131
	s_cmp_lg_u64 vcc, exec
	v_mov_b32_e32 v130, 1.0
	s_cbranch_scc1 .LBB0_868

; __device__ __forceinline__ void qkt64c(f32x16& p0, f32x16& p1, const char* Ks, const bf16x8* qr, const f32x16& cinit, int r32, int hi) {
; #pragma unroll
;     for (int d0 = 0; d0 < 4; ++d0) { const int cb = (d0 * 16 + hi * 8) * 2;
;         const bf16x8 b0 = *reinterpret_cast<const bf16x8*>(Ks + kswz<64>(r32, cb));
;         const bf16x8 b1 = *reinterpret_cast<const bf16x8*>(Ks + kswz<64>(32 + r32, cb));
;         if (d0 == 0) { p0 = __builtin_amdgcn_mfma_f32_32x32x16_bf16(b0, qr[0], cinit, 0, 0, 0); p1 = __builtin_amdgcn_mfma_f32_32x32x16_bf16(b1, qr[0], cinit, 0, 0, 0); }
;         else { p0 = __builtin_amdgcn_mfma_f32_32x32x16_bf16(b0, qr[d0], p0, 0, 0, 0); p1 = __builtin_amdgcn_mfma_f32_32x32x16_bf16(b1, qr[d0], p1, 0, 0, 0); } }
; }
.LBB0_846:
	v_lshl_add_u64 v[202:203], v[200:201], 0, s[64:65]
	s_mov_b32 s2, 0x8a40000
	v_add_co_u32_e32 v64, vcc, s2, v202
	s_mov_b32 s2, 0x8a50000
	s_nop 0
	v_addc_co_u32_e32 v65, vcc, 0, v203, vcc
	v_add_co_u32_e32 v66, vcc, s2, v202
	v_lshl_add_u64 v[204:205], v[198:199], 0, s[64:65]
	s_nop 0
	v_addc_co_u32_e32 v67, vcc, 0, v203, vcc
	s_mov_b32 s2, 0x6a40000
	global_load_dwordx4 v[178:181], v[64:65], off
	global_load_dwordx4 v[182:185], v[66:67], off
	v_add_co_u32_e32 v64, vcc, s2, v204
	s_nop 1
	v_addc_co_u32_e32 v65, vcc, 0, v205, vcc
	global_load_dwordx4 v[186:189], v[64:65], off offset:128
	s_lshl_b32 s2, s30, 13
	s_add_i32 s2, s2, 0
	v_add_u32_e32 v128, s2, v227
	ds_read_b128 v[190:193], v128 offset:53248
	ds_read_b128 v[144:147], v128 offset:49152
	v_exp_f32_e32 v208, v120
	v_exp_f32_e32 v209, v121
	v_add_f32_e32 v120, v96, v97
	v_add_f32_e32 v121, v98, v99
	s_waitcnt lgkmcnt(0)
	v_mfma_f32_32x32x16_bf16 v[128:143], v[144:147], v[162:165], v[80:95]
	v_add_u32_e32 v144, s2, v231
	ds_read_b128 v[236:239], v144 offset:53248
	ds_read_b128 v[144:147], v144 offset:49152
	v_exp_f32_e32 v210, v122
	v_add_f32_e32 v120, v120, v121
	v_add_f32_e32 v121, v100, v101
	v_add_f32_e32 v122, v102, v103
	v_exp_f32_e32 v211, v123
	s_waitcnt lgkmcnt(0)
	v_mfma_f32_32x32x16_bf16 v[128:143], v[144:147], v[166:169], v[128:143]
	v_add_u32_e32 v144, s2, v232
	ds_read_b128 v[240:243], v144 offset:53248
	ds_read_b128 v[144:147], v144 offset:49152
	v_add_f32_e32 v121, v121, v122
	v_add_f32_e32 v122, v104, v105
	v_add_f32_e32 v123, v106, v107
	v_add_f32_e32 v122, v122, v123
	v_add_f32_e32 v123, v108, v109
	s_waitcnt lgkmcnt(0)
	v_mfma_f32_32x32x16_bf16 v[128:143], v[144:147], v[170:173], v[128:143]
	v_add_u32_e32 v144, s2, v233
	ds_read_b128 v[244:247], v144 offset:53248
	ds_read_b128 v[144:147], v144 offset:49152
	v_exp_f32_e32 v124, v124
	v_exp_f32_e32 v125, v125
	v_exp_f32_e32 v126, v126
	v_exp_f32_e32 v127, v127
	v_cvt_pk_bf16_f32 v96, v96, v97
	s_waitcnt lgkmcnt(0)
	v_mfma_f32_32x32x16_bf16 v[128:143], v[144:147], v[174:177], v[128:143]
	v_cvt_pk_bf16_f32 v97, v98, v99
	v_cvt_pk_bf16_f32 v98, v100, v101
	v_cvt_pk_bf16_f32 v99, v102, v103
	s_nop 0
	v_permlane32_swap_b32_e32 v96, v98
	v_mfma_f32_32x32x16_bf16 v[144:159], v[190:193], v[162:165], v[80:95]
	v_add_f32_e32 v190, v110, v111
	v_add_f32_e32 v123, v123, v190
	v_add_f32_e32 v190, v112, v113
	v_add_f32_e32 v191, v114, v115
	v_add_f32_e32 v190, v190, v191
	v_add_f32_e32 v120, v190, v120
	v_add_f32_e32 v190, v116, v117
	v_mfma_f32_32x32x16_bf16 v[144:159], v[236:239], v[166:169], v[144:159]
	v_add_f32_e32 v191, v118, v119
	v_add_f32_e32 v190, v190, v191
	v_add_f32_e32 v121, v190, v121
	v_add_f32_e32 v190, v208, v209
	v_add_f32_e32 v191, v210, v211
	v_add_f32_e32 v190, v190, v191
	v_add_f32_e32 v122, v122, v190
	v_mfma_f32_32x32x16_bf16 v[144:159], v[240:243], v[170:173], v[144:159]
	v_add_f32_e32 v190, v124, v125
	v_add_f32_e32 v191, v126, v127
	v_add_f32_e32 v190, v190, v191
	v_add_f32_e32 v123, v123, v190
	v_add_f32_e32 v120, v120, v121
	v_add_f32_e32 v121, v122, v123
	v_add_f32_e32 v235, v120, v121
	v_mfma_f32_32x32x16_bf16 v[144:159], v[244:247], v[174:177], v[144:159]
	v_mov_b32_e32 v236, v235
	v_cvt_pk_bf16_f32 v120, v104, v105
	v_cvt_pk_bf16_f32 v121, v106, v107
	v_cvt_pk_bf16_f32 v122, v108, v109
	v_cvt_pk_bf16_f32 v123, v110, v111
	v_cvt_pk_bf16_f32 v104, v112, v113
	v_cvt_pk_bf16_f32 v105, v114, v115
	v_cvt_pk_bf16_f32 v106, v116, v117
	v_cvt_pk_bf16_f32 v107, v118, v119
	v_cvt_pk_bf16_f32 v100, v208, v209
	v_cvt_pk_bf16_f32 v101, v210, v211
	v_cvt_pk_bf16_f32 v102, v124, v125
	v_cvt_pk_bf16_f32 v103, v126, v127
	s_nop 1
	v_permlane32_swap_b32_e32 v235, v236
	v_permlane32_swap_b32_e32 v97, v99
	v_permlane32_swap_b32_e32 v120, v122
	v_permlane32_swap_b32_e32 v121, v123
	v_permlane32_swap_b32_e32 v104, v106
	v_permlane32_swap_b32_e32 v105, v107
	v_permlane32_swap_b32_e32 v100, v102
	v_permlane32_swap_b32_e32 v101, v103
	v_lshl_add_u32 v238, s12, 14, v221
	ds_read_b64_tr_b16 v[108:109], v238 offset:0
	ds_read_b64_tr_b16 v[110:111], v238 offset:0x800
	ds_read_b64_tr_b16 v[112:113], v238 offset:0x1000
	ds_read_b64_tr_b16 v[114:115], v238 offset:0x1800
	ds_read_b64_tr_b16 v[116:117], v238 offset:0x2000
	ds_read_b64_tr_b16 v[118:119], v238 offset:0x2800
	ds_read_b64_tr_b16 v[124:125], v238 offset:0x3000
	ds_read_b64_tr_b16 v[126:127], v238 offset:0x3800
	ds_read_b64_tr_b16 v[190:191], v238 offset:0x200
	ds_read_b64_tr_b16 v[192:193], v238 offset:0xa00
	ds_read_b64_tr_b16 v[240:241], v238 offset:0x1200
	ds_read_b64_tr_b16 v[242:243], v238 offset:0x1a00
	ds_read_b64_tr_b16 v[244:245], v238 offset:0x2200
	ds_read_b64_tr_b16 v[246:247], v238 offset:0x2a00
	ds_read_b64_tr_b16 v[208:209], v238 offset:0x3200
	ds_read_b64_tr_b16 v[210:211], v238 offset:0x3a00
	s_waitcnt lgkmcnt(8)
	s_nop 0
	v_mfma_f32_32x32x16_bf16 v[0:15], v[96:99], v[108:111], v[0:15]
	v_max_f32_e32 v108, v128, v129
	v_max3_f32 v108, v108, v144, v146
	v_max3_f32 v109, v130, v131, v145
	v_max3_f32 v108, v108, v147, v132
	v_max3_f32 v109, v109, v134, v135
	v_mfma_f32_32x32x16_bf16 v[0:15], v[120:123], v[112:115], v[0:15]
	v_max3_f32 v237, v108, v133, v148
	v_max3_f32 v239, v109, v150, v151
	v_mfma_f32_32x32x16_bf16 v[0:15], v[104:107], v[116:119], v[0:15]
	v_mfma_f32_32x32x16_bf16 v[0:15], v[100:103], v[124:127], v[0:15]
	ds_read_b64_tr_b16 v[124:125], v238 offset:0x400
	ds_read_b64_tr_b16 v[126:127], v238 offset:0xc00
	ds_read_b64_tr_b16 v[116:117], v238 offset:0x1400
	ds_read_b64_tr_b16 v[118:119], v238 offset:0x1c00
	ds_read_b64_tr_b16 v[112:113], v238 offset:0x2400
	ds_read_b64_tr_b16 v[114:115], v238 offset:0x2c00
	ds_read_b64_tr_b16 v[108:109], v238 offset:0x3400
	ds_read_b64_tr_b16 v[110:111], v238 offset:0x3c00
	s_waitcnt lgkmcnt(8)
	v_mfma_f32_32x32x16_bf16 v[48:63], v[96:99], v[190:193], v[48:63]
	v_max3_f32 v190, v237, v149, v136
	v_max3_f32 v191, v239, v138, v139
	v_max3_f32 v190, v190, v137, v152
	v_max3_f32 v191, v191, v154, v155
	v_max3_f32 v190, v190, v153, v140
	v_max3_f32 v191, v191, v142, v143
	v_max3_f32 v190, v190, v141, v156
	v_mfma_f32_32x32x16_bf16 v[48:63], v[120:123], v[240:243], v[48:63]
	v_max3_f32 v191, v191, v158, v159
	v_max3_f32 v190, v190, v157, v191
	v_mov_b32_e32 v191, v190
	s_nop 1
	v_permlane32_swap_b32_e32 v190, v191
	v_mfma_f32_32x32x16_bf16 v[48:63], v[104:107], v[244:247], v[48:63]
	v_max_f32_e32 v237, v190, v191
	v_mfma_f32_32x32x16_bf16 v[48:63], v[100:103], v[208:211], v[48:63]
	s_mov_b32 s2, 0x4138aa3b
	v_cmp_ge_f32_e32 vcc, s2, v237
	s_cmp_eq_u64 vcc, exec
	s_cbranch_scc0 .LBB0_859
	v_mov_b32_e32 v237, 1.0

; __device__ __forceinline__ void qkt64c(f32x16& p0, f32x16& p1, const char* Ks, const bf16x8* qr, const f32x16& cinit, int r32, int hi) {
; #pragma unroll
;     for (int d0 = 0; d0 < 4; ++d0) { const int cb = (d0 * 16 + hi * 8) * 2;
;         const bf16x8 b0 = *reinterpret_cast<const bf16x8*>(Ks + kswz<64>(r32, cb));
;         const bf16x8 b1 = *reinterpret_cast<const bf16x8*>(Ks + kswz<64>(32 + r32, cb));
;         if (d0 == 0) { p0 = __builtin_amdgcn_mfma_f32_32x32x16_bf16(b0, qr[0], cinit, 0, 0, 0); p1 = __builtin_amdgcn_mfma_f32_32x32x16_bf16(b1, qr[0], cinit, 0, 0, 0); }
;         else { p0 = __builtin_amdgcn_mfma_f32_32x32x16_bf16(b0, qr[d0], p0, 0, 0, 0); p1 = __builtin_amdgcn_mfma_f32_32x32x16_bf16(b1, qr[d0], p1, 0, 0, 0); } }
; }
.LBB0_852:
	v_add_co_u32_e32 v96, vcc, 0x8a60000, v202
	s_waitcnt lgkmcnt(0)
	s_nop 0
	v_addc_co_u32_e32 v97, vcc, 0, v203, vcc
	v_add_co_u32_e32 v98, vcc, 0x8a70000, v202
	s_barrier
	s_nop 0
	v_addc_co_u32_e32 v99, vcc, 0, v203, vcc
	global_load_dwordx4 v[178:181], v[96:97], off
	global_load_dwordx4 v[182:185], v[98:99], off
	v_add_co_u32_e32 v96, vcc, 0x6a60000, v204
	s_nop 1
	v_addc_co_u32_e32 v97, vcc, 0, v205, vcc
	global_load_dwordx4 v[186:189], v[96:97], off offset:128
	v_add_u32_e32 v96, s2, v227
	ds_read_b128 v[190:193], v96 offset:53248
	ds_read_b128 v[112:115], v96 offset:49152
	v_exp_f32_e32 v242, v152
	v_exp_f32_e32 v243, v153
	v_add_f32_e32 v152, v128, v129
	v_add_f32_e32 v153, v130, v131
	s_waitcnt lgkmcnt(0)
	v_mfma_f32_32x32x16_bf16 v[96:111], v[112:115], v[162:165], v[80:95]
	v_add_u32_e32 v112, s2, v231
	ds_read_b128 v[202:205], v112 offset:53248
	ds_read_b128 v[112:115], v112 offset:49152
	v_exp_f32_e32 v244, v154
	v_add_f32_e32 v152, v152, v153
	v_add_f32_e32 v153, v132, v133
	v_add_f32_e32 v154, v134, v135
	v_exp_f32_e32 v245, v155
	s_waitcnt lgkmcnt(0)
	v_mfma_f32_32x32x16_bf16 v[96:111], v[112:115], v[166:169], v[96:111]
	v_add_u32_e32 v112, s2, v232
	ds_read_b128 v[208:211], v112 offset:53248
	ds_read_b128 v[112:115], v112 offset:49152
	v_add_f32_e32 v153, v153, v154
	v_add_f32_e32 v154, v136, v137
	v_add_f32_e32 v155, v138, v139
	v_add_f32_e32 v154, v154, v155
	v_add_f32_e32 v155, v140, v141
	s_waitcnt lgkmcnt(0)
	v_mfma_f32_32x32x16_bf16 v[96:111], v[112:115], v[170:173], v[96:111]
	v_add_u32_e32 v112, s2, v233
	ds_read_b128 v[238:241], v112 offset:53248
	ds_read_b128 v[112:115], v112 offset:49152
	v_exp_f32_e32 v156, v156
	v_exp_f32_e32 v157, v157
	v_exp_f32_e32 v158, v158
	v_exp_f32_e32 v159, v159
	s_waitcnt lgkmcnt(0)
	v_mfma_f32_32x32x16_bf16 v[96:111], v[112:115], v[174:177], v[96:111]
	v_mfma_f32_32x32x16_bf16 v[112:127], v[190:193], v[162:165], v[80:95]
	v_add_f32_e32 v190, v142, v143
	v_add_f32_e32 v155, v155, v190
	v_add_f32_e32 v190, v144, v145
	v_add_f32_e32 v191, v146, v147
	v_add_f32_e32 v190, v190, v191
	v_add_f32_e32 v152, v152, v190
	v_add_f32_e32 v190, v148, v149
	v_mfma_f32_32x32x16_bf16 v[112:127], v[202:205], v[166:169], v[112:127]
	v_add_f32_e32 v191, v150, v151
	v_add_f32_e32 v190, v190, v191
	v_add_f32_e32 v153, v153, v190
	v_add_f32_e32 v190, v242, v243
	v_add_f32_e32 v191, v244, v245
	v_add_f32_e32 v190, v190, v191
	v_add_f32_e32 v154, v154, v190
	v_mfma_f32_32x32x16_bf16 v[112:127], v[208:211], v[170:173], v[112:127]
	v_add_f32_e32 v190, v156, v157
	v_add_f32_e32 v191, v158, v159
	v_add_f32_e32 v190, v190, v191
	v_add_f32_e32 v155, v155, v190
	v_add_f32_e32 v152, v152, v153
	v_add_f32_e32 v153, v154, v155
	v_add_f32_e32 v203, v152, v153
	v_mfma_f32_32x32x16_bf16 v[112:127], v[238:241], v[174:177], v[112:127]
	v_mov_b32_e32 v204, v203
	v_cvt_pk_bf16_f32 v152, v128, v129
	v_cvt_pk_bf16_f32 v153, v130, v131
	v_cvt_pk_bf16_f32 v154, v132, v133
	v_cvt_pk_bf16_f32 v155, v134, v135
	v_cvt_pk_bf16_f32 v136, v136, v137
	v_cvt_pk_bf16_f32 v137, v138, v139
	v_cvt_pk_bf16_f32 v138, v140, v141
	v_cvt_pk_bf16_f32 v139, v142, v143
	v_cvt_pk_bf16_f32 v132, v144, v145
	v_cvt_pk_bf16_f32 v133, v146, v147
	v_cvt_pk_bf16_f32 v134, v148, v149
	v_cvt_pk_bf16_f32 v135, v150, v151
	v_cvt_pk_bf16_f32 v128, v242, v243
	v_cvt_pk_bf16_f32 v129, v244, v245
	v_cvt_pk_bf16_f32 v130, v156, v157
	v_cvt_pk_bf16_f32 v131, v158, v159
	s_nop 1
	v_permlane32_swap_b32_e32 v203, v204
	v_permlane32_swap_b32_e32 v152, v154
	v_permlane32_swap_b32_e32 v153, v155
	v_permlane32_swap_b32_e32 v136, v138
	v_permlane32_swap_b32_e32 v137, v139
	v_permlane32_swap_b32_e32 v132, v134
	v_permlane32_swap_b32_e32 v133, v135
	v_permlane32_swap_b32_e32 v128, v130
	v_permlane32_swap_b32_e32 v129, v131
	v_lshl_add_u32 v205, s30, 14, v221
	ds_read_b64_tr_b16 v[140:141], v205 offset:0
	ds_read_b64_tr_b16 v[142:143], v205 offset:0x800
	ds_read_b64_tr_b16 v[144:145], v205 offset:0x1000
	ds_read_b64_tr_b16 v[146:147], v205 offset:0x1800
	ds_read_b64_tr_b16 v[148:149], v205 offset:0x2000
	ds_read_b64_tr_b16 v[150:151], v205 offset:0x2800
	ds_read_b64_tr_b16 v[156:157], v205 offset:0x3000
	ds_read_b64_tr_b16 v[158:159], v205 offset:0x3800
	ds_read_b64_tr_b16 v[190:191], v205 offset:0x200
	ds_read_b64_tr_b16 v[192:193], v205 offset:0xa00
	ds_read_b64_tr_b16 v[208:209], v205 offset:0x1200
	ds_read_b64_tr_b16 v[210:211], v205 offset:0x1a00
	ds_read_b64_tr_b16 v[238:239], v205 offset:0x2200
	ds_read_b64_tr_b16 v[240:241], v205 offset:0x2a00
	ds_read_b64_tr_b16 v[242:243], v205 offset:0x3200
	ds_read_b64_tr_b16 v[244:245], v205 offset:0x3a00
	s_waitcnt lgkmcnt(8)
	s_nop 0
	v_mfma_f32_32x32x16_bf16 v[0:15], v[152:155], v[140:143], v[0:15]
	v_max_f32_e32 v140, v96, v97
	v_max3_f32 v140, v140, v112, v114
	v_max3_f32 v141, v98, v99, v113
	v_max3_f32 v140, v140, v115, v100
	v_max3_f32 v141, v141, v102, v103
	v_mfma_f32_32x32x16_bf16 v[0:15], v[136:139], v[144:147], v[0:15]
	v_max3_f32 v202, v140, v101, v116
	v_max3_f32 v246, v141, v118, v119
	v_mfma_f32_32x32x16_bf16 v[0:15], v[132:135], v[148:151], v[0:15]
	v_mfma_f32_32x32x16_bf16 v[0:15], v[128:131], v[156:159], v[0:15]
	ds_read_b64_tr_b16 v[156:157], v205 offset:0x400
	ds_read_b64_tr_b16 v[158:159], v205 offset:0xc00
	ds_read_b64_tr_b16 v[148:149], v205 offset:0x1400
	ds_read_b64_tr_b16 v[150:151], v205 offset:0x1c00
	ds_read_b64_tr_b16 v[144:145], v205 offset:0x2400
	ds_read_b64_tr_b16 v[146:147], v205 offset:0x2c00
	ds_read_b64_tr_b16 v[140:141], v205 offset:0x3400
	ds_read_b64_tr_b16 v[142:143], v205 offset:0x3c00
	s_waitcnt lgkmcnt(8)
	v_mfma_f32_32x32x16_bf16 v[48:63], v[152:155], v[190:193], v[48:63]
	v_max3_f32 v190, v202, v117, v104
	v_max3_f32 v191, v246, v106, v107
	v_max3_f32 v190, v190, v105, v120
	v_max3_f32 v191, v191, v122, v123
	v_max3_f32 v190, v190, v121, v108
	v_max3_f32 v191, v191, v110, v111
	v_max3_f32 v190, v190, v109, v124
	v_mfma_f32_32x32x16_bf16 v[48:63], v[136:139], v[208:211], v[48:63]
	v_max3_f32 v191, v191, v126, v127
	v_max3_f32 v190, v190, v125, v191
	v_mov_b32_e32 v191, v190
	s_nop 1
	v_permlane32_swap_b32_e32 v190, v191
	v_mfma_f32_32x32x16_bf16 v[48:63], v[132:135], v[238:241], v[48:63]
	v_max_f32_e32 v238, v190, v191
	v_mfma_f32_32x32x16_bf16 v[48:63], v[128:131], v[242:245], v[48:63]
	s_mov_b32 s2, 0x4138aa3b
	v_cmp_ge_f32_e32 vcc, s2, v238
	s_cmp_eq_u64 vcc, exec
	v_mov_b32_e32 v202, 1.0
	s_cbranch_scc0 .LBB0_860

; __device__ __forceinline__ void qkt64c(f32x16& p0, f32x16& p1, const char* Ks, const bf16x8* qr, const f32x16& cinit, int r32, int hi) {
; #pragma unroll
;     for (int d0 = 0; d0 < 4; ++d0) { const int cb = (d0 * 16 + hi * 8) * 2;
;         const bf16x8 b0 = *reinterpret_cast<const bf16x8*>(Ks + kswz<64>(r32, cb));
;         const bf16x8 b1 = *reinterpret_cast<const bf16x8*>(Ks + kswz<64>(32 + r32, cb));
;         if (d0 == 0) { p0 = __builtin_amdgcn_mfma_f32_32x32x16_bf16(b0, qr[0], cinit, 0, 0, 0); p1 = __builtin_amdgcn_mfma_f32_32x32x16_bf16(b1, qr[0], cinit, 0, 0, 0); }
;         else { p0 = __builtin_amdgcn_mfma_f32_32x32x16_bf16(b0, qr[d0], p0, 0, 0, 0); p1 = __builtin_amdgcn_mfma_f32_32x32x16_bf16(b1, qr[d0], p1, 0, 0, 0); } }
; }
.LBB0_861:
	v_mov_b64_e32 v[64:65], v[80:81]
	v_mov_b64_e32 v[66:67], v[82:83]
	v_mov_b64_e32 v[68:69], v[84:85]
	v_mov_b64_e32 v[70:71], v[86:87]
	v_mov_b64_e32 v[72:73], v[88:89]
	v_mov_b64_e32 v[74:75], v[90:91]
	v_mov_b64_e32 v[76:77], v[92:93]
	v_mov_b64_e32 v[78:79], v[94:95]
	ds_read_b128 v[128:131], v226 offset:61440
	ds_read_b128 v[132:135], v226 offset:57344
	v_exp_f32_e32 v124, v124
	v_exp_f32_e32 v125, v125
	v_exp_f32_e32 v126, v126
	v_exp_f32_e32 v127, v127
	s_waitcnt lgkmcnt(0)
	v_mfma_f32_32x32x16_bf16 v[80:95], v[132:135], v[162:165], v[64:79]
	ds_read_b128 v[132:135], v228 offset:61440
	ds_read_b128 v[136:139], v228 offset:57344
	s_waitcnt lgkmcnt(0)
	v_mfma_f32_32x32x16_bf16 v[80:95], v[136:139], v[166:169], v[80:95]
	ds_read_b128 v[136:139], v229 offset:61440
	ds_read_b128 v[140:143], v229 offset:57344
	v_mfma_f32_32x32x16_bf16 v[64:79], v[128:131], v[162:165], v[64:79]
	v_add_f32_e32 v128, v110, v111
	v_add_f32_e32 v129, v114, v115
	s_waitcnt lgkmcnt(0)
	v_mfma_f32_32x32x16_bf16 v[80:95], v[140:143], v[170:173], v[80:95]
	ds_read_b128 v[140:143], v230 offset:61440
	ds_read_b128 v[144:147], v230 offset:57344
	v_mfma_f32_32x32x16_bf16 v[64:79], v[132:135], v[166:169], v[64:79]
	s_waitcnt lgkmcnt(0)
	v_mfma_f32_32x32x16_bf16 v[80:95], v[144:147], v[174:177], v[80:95]
	v_exp_f32_e32 v144, v120
	v_exp_f32_e32 v145, v121
	v_add_f32_e32 v120, v96, v97
	v_add_f32_e32 v121, v98, v99
	v_exp_f32_e32 v146, v122
	v_add_f32_e32 v120, v120, v121
	v_add_f32_e32 v121, v100, v101
	v_mfma_f32_32x32x16_bf16 v[64:79], v[136:139], v[170:173], v[64:79]
	v_add_f32_e32 v122, v102, v103
	v_exp_f32_e32 v147, v123
	v_add_f32_e32 v121, v121, v122
	v_add_f32_e32 v122, v104, v105
	v_add_f32_e32 v123, v106, v107
	v_add_f32_e32 v122, v122, v123
	v_add_f32_e32 v123, v108, v109
	v_add_f32_e32 v123, v123, v128
	v_add_f32_e32 v128, v112, v113
	v_add_f32_e32 v128, v128, v129
	v_add_f32_e32 v120, v120, v128
	v_add_f32_e32 v128, v116, v117
	v_add_f32_e32 v129, v118, v119
	v_add_f32_e32 v128, v128, v129
	v_add_f32_e32 v121, v121, v128
	v_add_f32_e32 v128, v144, v145
	v_add_f32_e32 v129, v146, v147
	v_mfma_f32_32x32x16_bf16 v[64:79], v[140:143], v[174:177], v[64:79]
	v_add_f32_e32 v128, v128, v129
	v_add_f32_e32 v122, v122, v128
	v_add_f32_e32 v128, v124, v125
	v_add_f32_e32 v129, v126, v127
	v_add_f32_e32 v128, v128, v129
	v_add_f32_e32 v123, v123, v128
	v_add_f32_e32 v120, v120, v121
	v_add_f32_e32 v121, v122, v123
	v_add_f32_e32 v128, v120, v121
	v_mov_b32_e32 v129, v128
	v_cvt_pk_bf16_f32 v96, v96, v97
	v_cvt_pk_bf16_f32 v97, v98, v99
	v_cvt_pk_bf16_f32 v98, v100, v101
	v_cvt_pk_bf16_f32 v99, v102, v103
	v_cvt_pk_bf16_f32 v120, v104, v105
	v_cvt_pk_bf16_f32 v121, v106, v107
	v_cvt_pk_bf16_f32 v122, v108, v109
	v_cvt_pk_bf16_f32 v123, v110, v111
	v_cvt_pk_bf16_f32 v104, v112, v113
	v_cvt_pk_bf16_f32 v105, v114, v115
	v_cvt_pk_bf16_f32 v106, v116, v117
	v_cvt_pk_bf16_f32 v107, v118, v119
	v_cvt_pk_bf16_f32 v100, v144, v145
	v_cvt_pk_bf16_f32 v101, v146, v147
	v_cvt_pk_bf16_f32 v102, v124, v125
	v_cvt_pk_bf16_f32 v103, v126, v127
	s_nop 1
	v_permlane32_swap_b32_e32 v128, v129
	v_permlane32_swap_b32_e32 v96, v98
	v_permlane32_swap_b32_e32 v97, v99
	v_permlane32_swap_b32_e32 v120, v122
	v_permlane32_swap_b32_e32 v121, v123
	v_permlane32_swap_b32_e32 v104, v106
	v_permlane32_swap_b32_e32 v105, v107
	v_permlane32_swap_b32_e32 v100, v102
	v_permlane32_swap_b32_e32 v101, v103
	ds_read_b64_tr_b16 v[108:109], v221 offset:0
	ds_read_b64_tr_b16 v[110:111], v221 offset:0x800
	ds_read_b64_tr_b16 v[112:113], v221 offset:0x1000
	ds_read_b64_tr_b16 v[114:115], v221 offset:0x1800
	ds_read_b64_tr_b16 v[116:117], v221 offset:0x2000
	ds_read_b64_tr_b16 v[118:119], v221 offset:0x2800
	ds_read_b64_tr_b16 v[124:125], v221 offset:0x3000
	ds_read_b64_tr_b16 v[126:127], v221 offset:0x3800
	ds_read_b64_tr_b16 v[130:131], v221 offset:0x200
	ds_read_b64_tr_b16 v[132:133], v221 offset:0xa00
	ds_read_b64_tr_b16 v[134:135], v221 offset:0x1200
	ds_read_b64_tr_b16 v[136:137], v221 offset:0x1a00
	ds_read_b64_tr_b16 v[138:139], v221 offset:0x2200
	ds_read_b64_tr_b16 v[140:141], v221 offset:0x2a00
	ds_read_b64_tr_b16 v[142:143], v221 offset:0x3200
	ds_read_b64_tr_b16 v[144:145], v221 offset:0x3a00
	s_waitcnt lgkmcnt(8)
	s_nop 0
	v_mfma_f32_32x32x16_bf16 v[0:15], v[96:99], v[108:111], v[0:15]
	v_max_f32_e32 v108, v81, v81
	v_max_f32_e32 v109, v80, v80
	v_max_f32_e32 v108, v109, v108
	v_max3_f32 v109, v82, v83, v65
	v_max3_f32 v108, v108, v64, v66
	v_max3_f32 v108, v108, v67, v84
	v_max3_f32 v109, v109, v86, v87
	v_mfma_f32_32x32x16_bf16 v[0:15], v[120:123], v[112:115], v[0:15]
	v_max3_f32 v146, v108, v85, v68
	v_max3_f32 v147, v109, v70, v71
	v_mfma_f32_32x32x16_bf16 v[0:15], v[104:107], v[116:119], v[0:15]
	v_mfma_f32_32x32x16_bf16 v[0:15], v[100:103], v[124:127], v[0:15]
	ds_read_b64_tr_b16 v[124:125], v221 offset:0x400
	ds_read_b64_tr_b16 v[126:127], v221 offset:0xc00
	ds_read_b64_tr_b16 v[116:117], v221 offset:0x1400
	ds_read_b64_tr_b16 v[118:119], v221 offset:0x1c00
	ds_read_b64_tr_b16 v[112:113], v221 offset:0x2400
	ds_read_b64_tr_b16 v[114:115], v221 offset:0x2c00
	ds_read_b64_tr_b16 v[108:109], v221 offset:0x3400
	ds_read_b64_tr_b16 v[110:111], v221 offset:0x3c00
	s_waitcnt lgkmcnt(8)
	v_mfma_f32_32x32x16_bf16 v[48:63], v[96:99], v[130:133], v[48:63]
	v_max3_f32 v130, v146, v69, v88
	v_max3_f32 v131, v147, v90, v91
	v_max3_f32 v130, v130, v89, v72
	v_max3_f32 v131, v131, v74, v75
	v_max3_f32 v130, v130, v73, v92
	v_max3_f32 v131, v131, v94, v95
	v_max3_f32 v130, v130, v93, v76
	v_mfma_f32_32x32x16_bf16 v[48:63], v[120:123], v[134:137], v[48:63]
	v_max3_f32 v131, v131, v78, v79
	v_max3_f32 v130, v130, v77, v131
	v_mov_b32_e32 v131, v130
	s_nop 1
	v_permlane32_swap_b32_e32 v130, v131
	v_max_f32_e32 v131, v131, v131
	v_max_f32_e32 v130, v130, v130
	v_mfma_f32_32x32x16_bf16 v[48:63], v[104:107], v[138:141], v[48:63]
	v_max_f32_e32 v131, v130, v131
	v_mfma_f32_32x32x16_bf16 v[48:63], v[100:103], v[142:145], v[48:63]
	s_mov_b32 s2, 0x4138aa3b
	v_cmp_ge_f32_e32 vcc, s2, v131
	s_cmp_lg_u64 vcc, exec
	v_mov_b32_e32 v130, 1.0
	v_mov_b64_e32 v[236:237], 0x100
	s_cbranch_scc1 .LBB0_869
